# sel max chain: dropped compiler s_nop 6 (distance already covered by the 16 ds_reads), 3 canonicalising v_max to 1, v_pk_add_f32 to two v_add_f32
# speedup vs baseline: 1.0256x; 1.0110x over previous
; __device__ __forceinline__ float xmax16(float v) { float a = v, b = v; PL_SWAP16(a, b); return fmaxf(a, b); }
; __device__ __forceinline__ float xmax32(float v) { float a = v, b = v; PL_SWAP32(a, b); return fmaxf(a, b); }
; template <class G> __device__ __forceinline__ void online_sm8(f32x4 (&s)[4], G& g, const float ref) {
;     float mx = s[0][0];
; #pragma unroll
;     for (int T_ = 0; T_ < 4; ++T_)
; #pragma unroll
;         for (int i = 0; i < 4; ++i) mx = fmaxf(mx, s[T_][i]);
;     const float t = mx + (ref - 5.f);
;     if (!__all(t <= g.m + SM_THR8)) {
;         const float mr = xmax32(xmax16(t));
;         const float mn = fmaxf(g.m, mr); const float al = __builtin_amdgcn_exp2f(g.m - mn); g.m = mn; g.l *= al;
; #pragma unroll
;         for (int dt = 0; dt < 8; ++dt) g.o[dt] = g.o[dt] * al;
;         const float d = ref - mn;
; #pragma unroll
;         for (int T_ = 0; T_ < 4; ++T_)
; #pragma unroll
;             for (int i = 0; i < 4; ++i) s[T_][i] += d;
;     }
.LBB0_1806:
	v_max_f32_e32 v18, v84, v85
	v_max3_f32 v18, v18, v86, v87
	v_max3_f32 v18, v18, v88, v89
	v_max3_f32 v18, v18, v90, v91
	v_max3_f32 v18, v18, v92, v93
	v_max3_f32 v18, v18, v94, v95
	v_max3_f32 v18, v18, v96, v97
	v_max3_f32 v114, v18, v98, v99
	v_add_f32_e32 v18, 0xc0a00000, v116
	v_add_f32_e32 v151, v19, v115
	v_add_f32_e32 v150, v18, v114
	v_cmp_le_f32_e32 vcc, v150, v151
	s_cmp_eq_u64 vcc, exec
	s_cbranch_scc1 .LBB0_1808
	v_mov_b32_e32 v18, v84
	v_mov_b32_e32 v84, v150
	s_nop 1
	v_permlane16_swap_b32 v84, v150
	v_mov_b32_e32 v151, v96
	v_max_f32_e32 v114, v150, v150
	v_max_f32_e32 v84, v84, v84
	v_max_f32_e32 v84, v84, v114
	v_mov_b32_e32 v114, v84
	s_nop 1
	v_permlane32_swap_b32 v114, v84
	v_mov_b32_e32 v150, v92
	v_max3_f32 v114, v19, v114, v84
	v_sub_f32_e32 v19, v19, v114
	v_exp_f32_e32 v84, v19
	v_mov_b32_e32 v19, v88
	v_mov_b32_e32 v210, v85
	v_mov_b32_e32 v211, v86
	v_mul_f32_e32 v183, v183, v84
	v_pk_mul_f32 v[82:83], v[82:83], v[84:85] op_sel_hi:[1,0]
	v_pk_mul_f32 v[80:81], v[80:81], v[84:85] op_sel_hi:[1,0]
	v_pk_mul_f32 v[78:79], v[78:79], v[84:85] op_sel_hi:[1,0]
	v_pk_mul_f32 v[76:77], v[76:77], v[84:85] op_sel_hi:[1,0]
	v_pk_mul_f32 v[74:75], v[74:75], v[84:85] op_sel_hi:[1,0]
	v_pk_mul_f32 v[72:73], v[72:73], v[84:85] op_sel_hi:[1,0]
	v_pk_mul_f32 v[70:71], v[70:71], v[84:85] op_sel_hi:[1,0]
	v_pk_mul_f32 v[68:69], v[68:69], v[84:85] op_sel_hi:[1,0]
	v_pk_mul_f32 v[66:67], v[66:67], v[84:85] op_sel_hi:[1,0]
	v_pk_mul_f32 v[64:65], v[64:65], v[84:85] op_sel_hi:[1,0]
	v_pk_mul_f32 v[62:63], v[62:63], v[84:85] op_sel_hi:[1,0]
	v_pk_mul_f32 v[60:61], v[60:61], v[84:85] op_sel_hi:[1,0]
	v_pk_mul_f32 v[58:59], v[58:59], v[84:85] op_sel_hi:[1,0]
	v_pk_mul_f32 v[56:57], v[56:57], v[84:85] op_sel_hi:[1,0]
	v_pk_mul_f32 v[54:55], v[54:55], v[84:85] op_sel_hi:[1,0]
	v_pk_mul_f32 v[52:53], v[52:53], v[84:85] op_sel_hi:[1,0]
	v_sub_f32_e32 v84, v116, v114
	v_pk_add_f32 v[212:213], v[18:19], v[84:85] op_sel_hi:[1,0]
	v_mov_b32_e32 v18, v89
	v_mov_b32_e32 v19, v90
	v_pk_add_f32 v[214:215], v[18:19], v[84:85] op_sel_hi:[1,0]
	v_mov_b32_e32 v18, v93
	v_mov_b32_e32 v19, v94
	v_pk_add_f32 v[88:89], v[18:19], v[84:85] op_sel_hi:[1,0]
	v_mov_b32_e32 v18, v97
	v_mov_b32_e32 v19, v98
	v_pk_add_f32 v[210:211], v[210:211], v[84:85] op_sel_hi:[1,0]
	v_pk_add_f32 v[150:151], v[150:151], v[84:85] op_sel_hi:[1,0]
	v_pk_add_f32 v[92:93], v[18:19], v[84:85] op_sel_hi:[1,0]
	v_add_f32_e32 v87, v87, v84
	v_add_f32_e32 v91, v91, v84
	v_add_f32_e32 v95, v95, v84
	v_add_f32_e32 v99, v99, v84
	v_mov_b32_e32 v19, v114
	v_mov_b32_e32 v97, v92
	v_mov_b32_e32 v98, v93
	v_mov_b32_e32 v93, v88
	v_mov_b32_e32 v94, v89
	v_mov_b32_e32 v89, v214
	v_mov_b32_e32 v90, v215
	v_mov_b32_e32 v85, v210
	v_mov_b32_e32 v86, v211
	v_mov_b32_e32 v84, v212
	v_mov_b32_e32 v88, v213
	v_mov_b32_e32 v92, v150
	v_mov_b32_e32 v96, v151

; __device__ __forceinline__ float xmax16(float v) { float a = v, b = v; PL_SWAP16(a, b); return fmaxf(a, b); }
; __device__ __forceinline__ float xmax32(float v) { float a = v, b = v; PL_SWAP32(a, b); return fmaxf(a, b); }
; template <class G> __device__ __forceinline__ void online_sm8(f32x4 (&s)[4], G& g, const float ref) {
;     float mx = s[0][0];
; #pragma unroll
;     for (int T_ = 0; T_ < 4; ++T_)
; #pragma unroll
;         for (int i = 0; i < 4; ++i) mx = fmaxf(mx, s[T_][i]);
;     const float t = mx + (ref - 5.f);
;     if (!__all(t <= g.m + SM_THR8)) {
;         const float mr = xmax32(xmax16(t));
;         const float mn = fmaxf(g.m, mr); const float al = __builtin_amdgcn_exp2f(g.m - mn); g.m = mn; g.l *= al;
; #pragma unroll
;         for (int dt = 0; dt < 8; ++dt) g.o[dt] = g.o[dt] * al;
;         const float d = ref - mn;
; #pragma unroll
;         for (int T_ = 0; T_ < 4; ++T_)
; #pragma unroll
;             for (int i = 0; i < 4; ++i) s[T_][i] += d;
;     }
.LBB0_1812:
	v_max_f32_e32 v114, v84, v85
	v_max3_f32 v114, v114, v86, v87
	v_max3_f32 v114, v114, v88, v89
	v_max3_f32 v114, v114, v90, v91
	v_max3_f32 v114, v114, v92, v93
	v_max3_f32 v114, v114, v94, v95
	v_max3_f32 v114, v114, v96, v97
	v_max3_f32 v114, v114, v98, v99
	v_add_f32_e32 v116, 0xc0a00000, v18
	v_add_f32_e32 v151, v117, v115
	v_add_f32_e32 v150, v116, v114
	v_cmp_le_f32_e32 vcc, v150, v151
	s_cmp_eq_u64 vcc, exec
	s_cbranch_scc1 .LBB0_1797
	v_mov_b32_e32 v116, v84
	v_mov_b32_e32 v84, v150
	s_nop 1
	v_permlane16_swap_b32 v150, v84
	v_mov_b32_e32 v151, v96
	v_max_f32_e32 v84, v84, v84
	v_max_f32_e32 v114, v150, v150
	v_max_f32_e32 v84, v114, v84
	v_mov_b32_e32 v114, v84
	s_nop 1
	v_permlane32_swap_b32 v84, v114
	v_mov_b32_e32 v150, v92
	v_max3_f32 v114, v117, v84, v114
	v_sub_f32_e32 v84, v117, v114
	v_exp_f32_e32 v84, v84
	v_sub_f32_e32 v18, v18, v114
	v_mov_b32_e32 v117, v88
	v_mov_b32_e32 v88, v93
	v_mul_f32_e32 v182, v182, v84
	v_pk_mul_f32 v[50:51], v[50:51], v[84:85] op_sel_hi:[1,0]
	v_pk_mul_f32 v[48:49], v[48:49], v[84:85] op_sel_hi:[1,0]
	v_pk_mul_f32 v[46:47], v[46:47], v[84:85] op_sel_hi:[1,0]
	v_pk_mul_f32 v[44:45], v[44:45], v[84:85] op_sel_hi:[1,0]
	v_pk_mul_f32 v[42:43], v[42:43], v[84:85] op_sel_hi:[1,0]
	v_pk_mul_f32 v[40:41], v[40:41], v[84:85] op_sel_hi:[1,0]
	v_pk_mul_f32 v[38:39], v[38:39], v[84:85] op_sel_hi:[1,0]
	v_pk_mul_f32 v[36:37], v[36:37], v[84:85] op_sel_hi:[1,0]
	v_pk_mul_f32 v[34:35], v[34:35], v[84:85] op_sel_hi:[1,0]
	v_pk_mul_f32 v[32:33], v[32:33], v[84:85] op_sel_hi:[1,0]
	v_pk_mul_f32 v[30:31], v[30:31], v[84:85] op_sel_hi:[1,0]
	v_pk_mul_f32 v[28:29], v[28:29], v[84:85] op_sel_hi:[1,0]
	v_pk_mul_f32 v[26:27], v[26:27], v[84:85] op_sel_hi:[1,0]
	v_pk_mul_f32 v[24:25], v[24:25], v[84:85] op_sel_hi:[1,0]
	v_pk_mul_f32 v[22:23], v[22:23], v[84:85] op_sel_hi:[1,0]
	v_pk_mul_f32 v[20:21], v[20:21], v[84:85] op_sel_hi:[1,0]
	v_mov_b32_e32 v84, v85
	v_mov_b32_e32 v85, v86
	v_pk_add_f32 v[210:211], v[84:85], v[18:19] op_sel_hi:[1,0]
	v_mov_b32_e32 v84, v89
	v_mov_b32_e32 v85, v90
	v_mov_b32_e32 v89, v94
	v_mov_b32_e32 v92, v97
	v_mov_b32_e32 v93, v98
	v_pk_add_f32 v[212:213], v[116:117], v[18:19] op_sel_hi:[1,0]
	v_pk_add_f32 v[84:85], v[84:85], v[18:19] op_sel_hi:[1,0]
	v_pk_add_f32 v[88:89], v[88:89], v[18:19] op_sel_hi:[1,0]
	v_pk_add_f32 v[150:151], v[150:151], v[18:19] op_sel_hi:[1,0]
	v_pk_add_f32 v[92:93], v[92:93], v[18:19] op_sel_hi:[1,0]
	v_add_f32_e32 v87, v87, v18
	v_add_f32_e32 v91, v91, v18
	v_add_f32_e32 v95, v95, v18
	v_add_f32_e32 v99, v99, v18
	v_mov_b32_e32 v117, v114
	v_mov_b32_e32 v97, v92
	v_mov_b32_e32 v98, v93
	v_mov_b32_e32 v93, v88
	v_mov_b32_e32 v94, v89
	v_mov_b32_e32 v89, v84
	v_mov_b32_e32 v90, v85
	v_mov_b32_e32 v85, v210
	v_mov_b32_e32 v86, v211
	v_mov_b32_e32 v84, v212
	v_mov_b32_e32 v88, v213
	v_mov_b32_e32 v92, v150
	v_mov_b32_e32 v96, v151
	s_branch .LBB0_1797
